# grid barrier: every workgroup starts the XCD L2 writeback before its arrival atomic (overlapping the atomic round trip); leader writeback kept (on v16)
# baseline (speedup 1.0000x reference)
.LBB0_85:
	s_mov_b64 s[38:39], exec
	v_mbcnt_lo_u32_b32 v1, s38, 0
	v_mbcnt_hi_u32_b32 v1, s39, v1
	v_cmp_eq_u32_e32 vcc, 0, v1
	s_and_saveexec_b64 s[28:29], vcc
	s_cbranch_execz .LBB0_87
	buffer_wbl2 sc1
	s_bcnt1_i32_b64 s4, s[38:39]
	v_mov_b32_e32 v4, s4
	v_readlane_b32 s4, v254, 43
	v_readlane_b32 s5, v254, 44
	s_nop 4
	global_atomic_add v4, v115, v4, s[4:5] sc0

.LBB0_236:
	s_mov_b64 s[28:29], exec
	v_mbcnt_lo_u32_b32 v1, s28, 0
	v_mbcnt_hi_u32_b32 v1, s29, v1
	v_cmp_eq_u32_e32 vcc, 0, v1
	s_and_saveexec_b64 s[26:27], vcc
	s_cbranch_execz .LBB0_238
	buffer_wbl2 sc1
	s_bcnt1_i32_b64 s4, s[28:29]
	v_mov_b32_e32 v4, s4
	v_readlane_b32 s4, v254, 43
	v_readlane_b32 s5, v254, 44
	s_nop 4
	global_atomic_add v4, v115, v4, s[4:5] sc0

.LBB0_411:
	s_mov_b64 s[26:27], exec
	v_mbcnt_lo_u32_b32 v1, s26, 0
	v_mbcnt_hi_u32_b32 v1, s27, v1
	v_cmp_eq_u32_e32 vcc, 0, v1
	s_and_saveexec_b64 s[10:11], vcc
	s_cbranch_execz .LBB0_413
	buffer_wbl2 sc1
	s_bcnt1_i32_b64 s4, s[26:27]
	v_mov_b32_e32 v4, s4
	v_readlane_b32 s4, v254, 43
	v_readlane_b32 s5, v254, 44
	s_nop 4
	global_atomic_add v4, v115, v4, s[4:5] sc0

.LBB0_567:
	s_mov_b64 s[28:29], exec
	v_mbcnt_lo_u32_b32 v1, s28, 0
	v_mbcnt_hi_u32_b32 v1, s29, v1
	v_cmp_eq_u32_e32 vcc, 0, v1
	s_and_saveexec_b64 s[10:11], vcc
	s_cbranch_execz .LBB0_569
	buffer_wbl2 sc1
	s_bcnt1_i32_b64 s4, s[28:29]
	v_mov_b32_e32 v4, s4
	v_readlane_b32 s4, v254, 43
	v_readlane_b32 s5, v254, 44
	s_nop 4
	global_atomic_add v4, v115, v4, s[4:5] sc0

.LBB0_1019:
	s_mov_b64 s[8:9], exec
	v_mbcnt_lo_u32_b32 v1, s8, 0
	v_mbcnt_hi_u32_b32 v1, s9, v1
	v_cmp_eq_u32_e32 vcc, 0, v1
	s_and_saveexec_b64 s[4:5], vcc
	s_cbranch_execz .LBB0_1021
	buffer_wbl2 sc1
	s_bcnt1_i32_b64 s7, s[8:9]
	v_readlane_b32 s8, v254, 43
	v_mov_b32_e32 v4, s7
	v_readlane_b32 s9, v254, 44
	s_nop 4
	global_atomic_add v4, v115, v4, s[8:9] sc0

.LBB0_1122:
	s_mov_b64 s[10:11], exec
	v_mbcnt_lo_u32_b32 v1, s10, 0
	v_mbcnt_hi_u32_b32 v1, s11, v1
	v_cmp_eq_u32_e32 vcc, 0, v1
	s_and_saveexec_b64 s[8:9], vcc
	s_cbranch_execz .LBB0_1124
	buffer_wbl2 sc1
	s_bcnt1_i32_b64 s7, s[10:11]
	v_readlane_b32 s10, v254, 43
	v_mov_b32_e32 v4, s7
	v_readlane_b32 s11, v254, 44
	s_nop 4
	global_atomic_add v4, v115, v4, s[10:11] sc0
